# baseline (speedup 1.0000x reference)
.LBB0_16:
	s_or_b64 exec, exec, s[0:1]
	s_mul_i32 s0, s23, 0x6200
	s_lshl_b32 s1, s6, 2
	s_add_i32 s0, s0, s1
	s_cmp_lg_u32 s23, 0
	s_cselect_b32 s1, 0xa000, 0
	s_add_i32 s0, s0, s1
	v_lshlrev_b32_e32 v14, 2, v134
	v_mul_u32_u24_e32 v15, 0xc40, v127
	v_add3_u32 v22, s0, v14, v15
	v_mov_b32_e32 v14, v50
	v_mov_b32_e32 v15, v62
	v_mov_b32_e32 v16, v66
	v_mov_b32_e32 v17, v10
	s_cmp_lg_u32 s23, 0
	s_cbranch_scc1 .Lseg_wr
	s_barrier
.Lseg_wr:
	ds_write_b128 v22, v[14:17]
	v_mov_b32_e32 v14, v51
	v_mov_b32_e32 v15, v63
	v_mov_b32_e32 v16, v67
	v_mov_b32_e32 v17, v11
	ds_write_b128 v22, v[14:17] offset:784
	v_mov_b32_e32 v17, v12
	v_mov_b32_e32 v10, v53
	v_mov_b32_e32 v11, v65
	v_mov_b32_e32 v12, v69
	ds_write_b128 v22, v[10:13] offset:2352
	v_mov_b32_e32 v10, v18
	v_mov_b32_e32 v11, v30
	v_mov_b32_e32 v12, v46
	v_mov_b32_e32 v13, v6
	ds_write_b128 v22, v[10:13] offset:12544
	v_mov_b32_e32 v10, v19
	v_mov_b32_e32 v11, v31
	v_mov_b32_e32 v12, v47
	v_mov_b32_e32 v13, v7
	v_or_b32_e32 v1, s25, v1
	v_mov_b32_e32 v14, v52
	v_mov_b32_e32 v15, v64
	v_mov_b32_e32 v16, v68
	ds_write_b128 v22, v[10:13] offset:13328
	v_mov_b32_e32 v10, v20
	v_mov_b32_e32 v11, v32
	v_mov_b32_e32 v12, v48
	v_mov_b32_e32 v13, v8
	v_mov_b32_e32 v6, v21
	v_mov_b32_e32 v7, v33
	v_mov_b32_e32 v8, v49
	v_cmp_eq_u32_e32 vcc, 0, v1
	ds_write_b128 v22, v[14:17] offset:1568
	ds_write_b128 v22, v[10:13] offset:14112
	ds_write_b128 v22, v[6:9] offset:14896
	s_and_saveexec_b64 s[0:1], vcc
	s_cbranch_execz .LBB0_18
	v_lshl_or_b32 v1, s23, 7, v129
	v_add_u32_e32 v1, 0x22800, v1
	ds_write_b128 v1, v[2:5]
	ds_write_b128 v1, v[78:81] offset:64
.LBB0_18:
	s_or_b64 exec, exec, s[0:1]
	s_and_b32 s0, s3, 0x3ffffffc
	v_and_b32_e32 v1, 31, v0
	v_and_b32_e32 v2, 0x3e0, v0
	s_movk_i32 s2, 0x310
	s_or_b32 s0, s0, s22
	v_mad_u32_u24 v26, v1, s2, v2
	s_cmp_lg_u32 s23, 0
	s_cbranch_scc0 .Lseg_rd
	s_waitcnt lgkmcnt(0)
	s_barrier
.Lseg_rd:
	v_add_u32_e32 v27, 0x10000, v26
	s_lshl_b32 s0, s0, 2
	ds_read_b128 v[10:13], v27 offset:512
	ds_read_b128 v[14:17], v27 offset:528
	ds_read_b128 v[18:21], v27 offset:25600
	ds_read_b128 v[22:25], v27 offset:25616
	ds_read_b128 v[34:37], v27 offset:50688
	ds_read_b128 v[38:41], v27 offset:50704
	s_or_b32 s0, s0, s24
	s_mul_hi_i32 s1, s0, 0x3000
	s_mulk_i32 s0, 0x3000
	s_add_u32 s0, s8, s0
	s_addc_u32 s1, s9, s1
	s_waitcnt lgkmcnt(0)
	s_barrier
	ds_read_b128 v[2:5], v26
	ds_read_b128 v[6:9], v26 offset:16
	v_mov_b32_e32 v1, 0
	s_cmp_eq_u32 s24, 0
	s_waitcnt lgkmcnt(0)
	v_pk_add_f32 v[8:9], v[8:9], 0 op_sel_hi:[1,0]
	v_pk_add_f32 v[4:5], v[4:5], 0 op_sel_hi:[1,0]
	v_pk_add_f32 v[6:7], v[6:7], 0 op_sel_hi:[1,0]
	v_pk_add_f32 v[2:3], v[2:3], 0 op_sel_hi:[1,0]
	v_pk_add_f32 v[4:5], v[4:5], v[12:13]
	v_pk_add_f32 v[8:9], v[8:9], v[16:17]
	v_pk_add_f32 v[2:3], v[2:3], v[10:11]
	v_pk_add_f32 v[6:7], v[6:7], v[14:15]
	v_pk_add_f32 v[8:9], v[8:9], v[24:25]
	v_pk_add_f32 v[4:5], v[4:5], v[20:21]
	v_pk_add_f32 v[6:7], v[6:7], v[22:23]
	v_pk_add_f32 v[2:3], v[2:3], v[18:19]
	v_pk_add_f32 v[10:11], v[4:5], v[36:37]
	v_pk_add_f32 v[4:5], v[8:9], v[40:41]
	v_pk_add_f32 v[8:9], v[2:3], v[34:35]
	v_pk_add_f32 v[6:7], v[6:7], v[38:39]
	v_lshl_add_u64 v[12:13], v[0:1], 4, s[0:1]
	s_cselect_b64 s[0:1], -1, 0
	v_cmp_gt_u32_e32 vcc, 32, v0
	v_cvt_pk_bf16_f32 v5, v4, v5
	v_cvt_pk_bf16_f32 v3, v10, v11
	v_cvt_pk_bf16_f32 v4, v6, v7
	v_cvt_pk_bf16_f32 v2, v8, v9
	s_and_b64 s[0:1], s[0:1], vcc
	global_store_dwordx4 v[12:13], v[2:5], off sc0 sc1
	s_and_saveexec_b64 s[4:5], s[0:1]
	s_cbranch_execz .LBB0_20
	v_mov_b32_e32 v1, 0x22800
	v_lshl_add_u32 v1, v0, 2, v1
	ds_read2_b32 v[2:3], v1 offset1:32
	ds_read2_b32 v[4:5], v1 offset0:64 offset1:96
	v_lshl_or_b32 v0, s3, 5, v0
	v_ashrrev_i32_e32 v1, 31, v0
	v_lshl_add_u64 v[0:1], v[0:1], 2, s[10:11]
	s_waitcnt lgkmcnt(1)
	v_add_f32_e32 v2, 0, v2
	v_add_f32_e32 v2, v2, v3
	s_waitcnt lgkmcnt(0)
	v_add_f32_e32 v2, v2, v4
	v_add_f32_e32 v2, v2, v5
	global_store_dword v[0:1], v2, off sc0 sc1

	.amdhsa_kernel _Z14seg_sum_kernelPKfS0_S0_PDv8_DF16bS2_Pf
		.amdhsa_group_segment_fixed_size 141840
		.amdhsa_private_segment_fixed_size 0
		.amdhsa_kernarg_size 48
		.amdhsa_user_sgpr_count 2
		.amdhsa_user_sgpr_dispatch_ptr 0
		.amdhsa_user_sgpr_queue_ptr 0
		.amdhsa_user_sgpr_kernarg_segment_ptr 1
		.amdhsa_user_sgpr_dispatch_id 0
		.amdhsa_user_sgpr_kernarg_preload_length 0
		.amdhsa_user_sgpr_kernarg_preload_offset 0
		.amdhsa_user_sgpr_private_segment_size 0
		.amdhsa_uses_dynamic_stack 0
		.amdhsa_enable_private_segment 0
		.amdhsa_system_sgpr_workgroup_id_x 1
		.amdhsa_system_sgpr_workgroup_id_y 0
		.amdhsa_system_sgpr_workgroup_id_z 0
		.amdhsa_system_sgpr_workgroup_info 0
		.amdhsa_system_vgpr_workitem_id 0
		.amdhsa_next_free_vgpr 142
		.amdhsa_next_free_sgpr 96
		.amdhsa_accum_offset 144
		.amdhsa_reserve_vcc 1
		.amdhsa_float_round_mode_32 0
		.amdhsa_float_round_mode_16_64 0
		.amdhsa_float_denorm_mode_32 3
		.amdhsa_float_denorm_mode_16_64 3
		.amdhsa_dx10_clamp 1
		.amdhsa_ieee_mode 1
		.amdhsa_fp16_overflow 0
		.amdhsa_tg_split 0
		.amdhsa_exception_fp_ieee_invalid_op 0
		.amdhsa_exception_fp_denorm_src 0
		.amdhsa_exception_fp_ieee_div_zero 0
		.amdhsa_exception_fp_ieee_overflow 0
		.amdhsa_exception_fp_ieee_underflow 0
		.amdhsa_exception_fp_ieee_inexact 0
		.amdhsa_exception_int_div_zero 0
	.end_amdhsa_kernel

amdhsa.kernels:
  - .agpr_count:     0
    .args:
      - .actual_access:  read_only
        .address_space:  global
        .offset:         0
        .size:           8
        .value_kind:     global_buffer
      - .actual_access:  read_only
        .address_space:  global
        .offset:         8
        .size:           8
        .value_kind:     global_buffer
      - .actual_access:  read_only
        .address_space:  global
        .offset:         16
        .size:           8
        .value_kind:     global_buffer
      - .actual_access:  write_only
        .address_space:  global
        .offset:         24
        .size:           8
        .value_kind:     global_buffer
      - .actual_access:  write_only
        .address_space:  global
        .offset:         32
        .size:           8
        .value_kind:     global_buffer
      - .actual_access:  write_only
        .address_space:  global
        .offset:         40
        .size:           8
        .value_kind:     global_buffer
    .group_segment_fixed_size: 141840
    .kernarg_segment_align: 8
    .kernarg_segment_size: 48
    .language:       OpenCL C
    .language_version:
      - 2
      - 0
    .max_flat_workgroup_size: 768
    .name:           _Z14seg_sum_kernelPKfS0_S0_PDv8_DF16bS2_Pf
    .private_segment_fixed_size: 0
    .sgpr_count:     42
    .sgpr_spill_count: 0
    .symbol:         _Z14seg_sum_kernelPKfS0_S0_PDv8_DF16bS2_Pf.kd
    .uniform_work_group_size: 1
    .uses_dynamic_stack: false
    .vgpr_count:     142
    .vgpr_spill_count: 0
    .wavefront_size: 64
  - .agpr_count:     16
    .args:
      - .actual_access:  read_only
        .address_space:  global
        .offset:         0
        .size:           8
        .value_kind:     global_buffer
      - .actual_access:  read_only
        .address_space:  global
        .offset:         8
        .size:           8
        .value_kind:     global_buffer
      - .actual_access:  read_only
        .address_space:  global
        .offset:         16
        .size:           8
        .value_kind:     global_buffer
      - .actual_access:  read_only
        .address_space:  global
        .offset:         24
        .size:           8
        .value_kind:     global_buffer
      - .actual_access:  write_only
        .address_space:  global
        .offset:         32
        .size:           8
        .value_kind:     global_buffer
      - .actual_access:  write_only
        .address_space:  global
        .offset:         40
        .size:           8
        .value_kind:     global_buffer
      - .actual_access:  write_only
        .address_space:  global
        .offset:         48
        .size:           8
        .value_kind:     global_buffer
    .group_segment_fixed_size: 17152
    .kernarg_segment_align: 8
    .kernarg_segment_size: 56
    .language:       OpenCL C
    .language_version:
      - 2
      - 0
    .max_flat_workgroup_size: 256
    .name:           _Z13logits_kernelPKDv8_DF16bS1_PKfS3_PDv2_fS5_Pf
    .private_segment_fixed_size: 0
    .sgpr_count:     37
    .sgpr_spill_count: 0
    .symbol:         _Z13logits_kernelPKDv8_DF16bS1_PKfS3_PDv2_fS5_Pf.kd
    .uniform_work_group_size: 1
    .uses_dynamic_stack: false
    .vgpr_count:     268
    .vgpr_spill_count: 0
    .wavefront_size: 64
  - .agpr_count:     0
    .args:
      - .actual_access:  read_only
        .address_space:  global
        .offset:         0
        .size:           8
        .value_kind:     global_buffer
      - .actual_access:  read_only
        .address_space:  global
        .offset:         8
        .size:           8
        .value_kind:     global_buffer
      - .actual_access:  read_only
        .address_space:  global
        .offset:         16
        .size:           8
        .value_kind:     global_buffer
      - .actual_access:  read_only
        .address_space:  global
        .offset:         24
        .size:           8
        .value_kind:     global_buffer
      - .actual_access:  write_only
        .address_space:  global
        .offset:         32
        .size:           8
        .value_kind:     global_buffer
    .group_segment_fixed_size: 128
    .kernarg_segment_align: 8
    .kernarg_segment_size: 40
    .language:       OpenCL C
    .language_version:
      - 2
      - 0
    .max_flat_workgroup_size: 1024
    .name:           _Z12final_kernelPKDv4_fS1_PKfS3_Pf
    .private_segment_fixed_size: 0
    .sgpr_count:     20
    .sgpr_spill_count: 0
    .symbol:         _Z12final_kernelPKDv4_fS1_PKfS3_Pf.kd
    .uniform_work_group_size: 1
    .uses_dynamic_stack: false
    .vgpr_count:     52
    .vgpr_spill_count: 0
    .wavefront_size: 64
